# ILC6-nt + skip the now-empty conv_drain calls in phase 5 and the queue peek in p6 (queue is disabled)
# baseline (speedup 1.0000x reference)
; #define LAS __attribute__((address_space(3)))
; __device__ __forceinline__ unsigned xb_ld(unsigned* p)              { return __hip_atomic_load(p, __ATOMIC_RELAXED, __HIP_MEMORY_SCOPE_AGENT); }
; __device__ __forceinline__ unsigned xb_add(unsigned* p, unsigned v) { return __hip_atomic_fetch_add(p, v, __ATOMIC_RELAXED, __HIP_MEMORY_SCOPE_AGENT); }
;     __device__ __forceinline__ unsigned char* ws() const { return *(unsigned char* const __attribute__((address_space(4)))*)(p + 232); }
;     volatile LAS unsigned* st = (volatile LAS unsigned*)(lds + MISC_OFF) + 8;
;     unsigned* qw = (unsigned*)(ws + WS_CTL) + CW_Q;
;     int tl = tid_x(); asm volatile("" : "+v"(tl));
;     const int wave = __builtin_amdgcn_readfirstlane(tl >> 6), lane = tl & 63;
;     LAS float* scr = (LAS float*)(lds + wave * 16640);
;     __syncthreads();
;     unsigned ahead = 0xFFFFFFFFu;
;     if (tl == 0 && max_claims > 0) { if (xb_ld(qw) < (unsigned)target) ahead = xb_add(qw, 32u); }
;     for (int nc = 0; nc < max_claims; ++nc) {
;         if (tl == 0) { st[6] = ahead; if (ahead < (unsigned)target && nc + 1 < max_claims) ahead = (ahead + 32u < (unsigned)target) ? xb_add(qw, 32u) : 0xFFFFFFFFu; }
.LBB0_1234:
	v_readlane_b32 s0, v254, 60
	s_mul_i32 s22, s0, 0xc300
	s_add_i32 s20, s22, 0xc300
	s_add_u32 s4, s28, 0x20000
	s_getreg_b32 s0, hwreg(HW_REG_HW_ID, 0, 6)
	s_addc_u32 s5, s29, 0
	s_and_b32 s0, s0, 63
	s_lshl_b32 s0, s0, 2
	s_add_i32 s0, s0, 0
	s_add_i32 s0, s0, 0x23f00
	v_mov_b32_e32 v0, s0
	ds_read_b32 v0, v0
	v_mbcnt_lo_u32_b32 v1, -1, 0
	v_mbcnt_hi_u32_b32 v1, -1, v1
	v_readlane_b32 s1, v254, 61
	v_mov_b32_e32 v129, -1
	s_waitcnt lgkmcnt(0)
	v_readfirstlane_b32 s0, v0
	s_nop 1
	v_lshl_add_u32 v0, s0, 6, v1
	s_nop 0
	v_readfirstlane_b32 s10, v0
	v_cmp_eq_u32_e64 s[2:3], 0, v0
	s_barrier
	s_and_saveexec_b64 s[0:1], s[2:3]
	s_branch .LBB0_1239
	global_load_dword v1, v193, s[4:5] sc1
	v_mov_b32_e32 v129, -1
	s_waitcnt vmcnt(0)
	v_cmp_le_u32_e32 vcc, s20, v1
	s_cbranch_vccnz .LBB0_1239
	s_mov_b64 s[8:9], exec
	v_mbcnt_lo_u32_b32 v1, s8, 0
	v_mbcnt_hi_u32_b32 v1, s9, v1
	v_cmp_eq_u32_e32 vcc, 0, v1
	s_and_saveexec_b64 s[6:7], vcc
	s_cbranch_execz .LBB0_1238
	s_bcnt1_i32_b64 s8, s[8:9]
	s_lshl_b32 s8, s8, 5
	v_mov_b32_e32 v2, s8
	global_atomic_add v2, v193, v2, s[4:5] sc0
